# v39 + integer RNE bf16 pair packing replaced by v_cvt_pk_bf16_f32 in the spatial gating unit (LayerNorm pass and its epilogue)
# speedup vs baseline: 1.0131x; 1.0070x over previous
; #define LAS __attribute__((address_space(3)))
; __device__ __forceinline__ unsigned pk2(float lo, float hi) { return f2bf(lo) | (f2bf(hi) << 16); }
; #define SPROBE(k) do { const unsigned long long tn_ = __builtin_amdgcn_s_memrealtime(); if (blockIdx.x == 0 && threadIdx.x == 0) atomicAdd(probe_words + (k), (unsigned)(tn_ - tp0_)); tp0_ = tn_; } while (0)
; #define SPROBE(k) do {} while (0)
; __device__ __forceinline__ void sgu_unit(LAS unsigned char* lds, int unit, const bf16* U, const bf16* VG, const bf16* Wsb, const float* bs, const float* lng, const float* lnb, bf16* YA, const float* stat, int tid_in, int lane_in, int wave, unsigned* probe_words = nullptr) {
;     ...
;     LG[tid] = lgv;
;     {
;         const int rsub = lane >> 5, ps = lane & 31;
; #pragma unroll
;         for (int i = 0; i < 8; ++i) { const int q = wave * 8 + i, row = 2 * q + rsub;
;             const bf16* src = VG + (row0 + row) * GW + half * 256 + ((ps ^ sgu_xkey(row)) * 8);
;             __builtin_amdgcn_global_load_lds((const unsigned*)src, (LAS unsigned*)(VS + q * 1024), 16, 0, 0); }
;     }
;     asm volatile("s_waitcnt vmcnt(0)" ::: "memory");
;     __syncthreads();
;     SPROBE(5);
;     {
;         const int pc = tid & 31, rb = tid >> 5;
;         const f32x4s ga = *(const LAS f32x4s*)(LG + pc * 8), gb = *(const LAS f32x4s*)(LG + pc * 8 + 4), ba = *(const LAS f32x4s*)(LB + pc * 8), bb = *(const LAS f32x4s*)(LB + pc * 8 + 4);
; #pragma unroll
;         for (int it = 0; it < 8; ++it) { const int jr = it * 16 + rb; const float mu = MU[jr], rs = RS[jr];
;             LAS v4u* cp = (LAS v4u*)(VS + jr * 512 + ((pc ^ sgu_xkey(jr)) * 16));
;             const v4u w = *cp; v4u o;
;             o.x = pk2((__uint_as_float(w.x << 16) - mu) * rs * ga[0] + ba[0], (__uint_as_float(w.x & 0xffff0000u) - mu) * rs * ga[1] + ba[1]);
;             o.y = pk2((__uint_as_float(w.y << 16) - mu) * rs * ga[2] + ba[2], (__uint_as_float(w.y & 0xffff0000u) - mu) * rs * ga[3] + ba[3]);
;             o.z = pk2((__uint_as_float(w.z << 16) - mu) * rs * gb[0] + bb[0], (__uint_as_float(w.z & 0xffff0000u) - mu) * rs * gb[1] + bb[1]);
;             o.w = pk2((__uint_as_float(w.w << 16) - mu) * rs * gb[2] + bb[2], (__uint_as_float(w.w & 0xffff0000u) - mu) * rs * gb[3] + bb[3]);
;             *cp = o; }
.LBB0_993:
	s_or_b64 exec, exec, s[0:1]
	v_lshl_add_u32 v70, v130, 2, 0
	v_lshrrev_b32_e32 v74, 5, v68
	s_waitcnt vmcnt(0)
	ds_write_b32 v70, v69 offset:1024
	v_or_b32_e32 v70, s35, v74
	v_ashrrev_i32_e32 v71, 31, v70
	v_and_b32_e32 v84, 31, v130
	v_lshl_add_u64 v[70:71], s[64:65], 0, v[70:71]
	v_lshlrev_b64 v[70:71], 10, v[70:71]
	v_lshlrev_b32_e32 v69, 4, v84
	v_lshl_add_u64 v[70:71], s[82:83], 0, v[70:71]
	v_bitop3_b32 v68, v68, v69, 32 bitop3:0x6c
	v_mov_b32_e32 v69, v3
	v_lshl_add_u64 v[70:71], v[70:71], 0, v[68:69]
	s_mov_b32 m0, s59
	v_readlane_b32 s0, v255, 41
	global_load_lds_dwordx4 v[70:71], off
	v_or_b32_e32 v70, s31, v74
	v_ashrrev_i32_e32 v71, 31, v70
	v_lshl_add_u64 v[72:73], s[64:65], 0, v[70:71]
	v_lshlrev_b32_e32 v70, 1, v70
	v_lshlrev_b64 v[72:73], 10, v[72:73]
	v_bitop3_b32 v70, v70, v84, 6 bitop3:0x6c
	v_lshl_add_u64 v[72:73], s[82:83], 0, v[72:73]
	v_lshlrev_b32_e32 v70, 4, v70
	v_mov_b32_e32 v71, v3
	v_lshl_add_u64 v[70:71], v[72:73], 0, v[70:71]
	s_mov_b32 m0, s92
	v_ashrrev_i32_e32 v85, 5, v130
	global_load_lds_dwordx4 v[70:71], off
	v_or_b32_e32 v70, s88, v74
	v_ashrrev_i32_e32 v71, 31, v70
	v_lshl_add_u64 v[70:71], s[64:65], 0, v[70:71]
	v_lshlrev_b64 v[70:71], 10, v[70:71]
	v_lshl_add_u64 v[70:71], s[82:83], 0, v[70:71]
	v_lshl_add_u64 v[68:69], v[70:71], 0, v[68:69]
	s_mov_b32 m0, s94
	v_lshlrev_b32_e32 v86, 1, v85
	global_load_lds_dwordx4 v[68:69], off
	v_or_b32_e32 v68, s58, v74
	v_ashrrev_i32_e32 v69, 31, v68
	v_lshl_add_u64 v[70:71], s[64:65], 0, v[68:69]
	v_lshlrev_b32_e32 v68, 1, v68
	v_lshlrev_b64 v[70:71], 10, v[70:71]
	v_bitop3_b32 v68, v68, v84, 6 bitop3:0x6c
	v_lshl_add_u64 v[70:71], s[82:83], 0, v[70:71]
	v_lshlrev_b32_e32 v68, 4, v68
	v_mov_b32_e32 v69, v3
	v_lshl_add_u64 v[68:69], v[70:71], 0, v[68:69]
	s_mov_b32 m0, s96
	v_lshlrev_b32_e32 v70, 1, v74
	global_load_lds_dwordx4 v[68:69], off
	v_or_b32_e32 v68, s89, v74
	v_ashrrev_i32_e32 v69, 31, v68
	v_lshl_add_u64 v[68:69], s[64:65], 0, v[68:69]
	v_lshlrev_b64 v[68:69], 10, v[68:69]
	v_bitop3_b32 v70, v70, v84, 8 bitop3:0x36
	v_lshl_add_u64 v[68:69], s[82:83], 0, v[68:69]
	v_lshlrev_b32_e32 v70, 4, v70
	v_mov_b32_e32 v71, v3
	v_lshl_add_u64 v[68:69], v[68:69], 0, v[70:71]
	s_mov_b32 m0, s0
	v_readlane_b32 s0, v255, 42
	global_load_lds_dwordx4 v[68:69], off
	v_or_b32_e32 v68, s84, v74
	v_ashrrev_i32_e32 v69, 31, v68
	v_lshl_add_u64 v[72:73], s[64:65], 0, v[68:69]
	v_lshlrev_b32_e32 v68, 1, v68
	v_and_b32_e32 v68, 6, v68
	v_lshlrev_b64 v[72:73], 10, v[72:73]
	v_bitop3_b32 v68, v68, v84, 8 bitop3:0x36
	v_lshl_add_u64 v[72:73], s[82:83], 0, v[72:73]
	v_lshlrev_b32_e32 v68, 4, v68
	v_mov_b32_e32 v69, v3
	v_lshl_add_u64 v[68:69], v[72:73], 0, v[68:69]
	s_mov_b32 m0, s0
	v_readlane_b32 s0, v255, 31
	global_load_lds_dwordx4 v[68:69], off
	v_or_b32_e32 v68, s85, v74
	v_ashrrev_i32_e32 v69, 31, v68
	v_lshl_add_u64 v[68:69], s[64:65], 0, v[68:69]
	v_lshlrev_b64 v[68:69], 10, v[68:69]
	v_lshl_add_u64 v[68:69], s[82:83], 0, v[68:69]
	v_lshl_add_u64 v[68:69], v[68:69], 0, v[70:71]
	s_mov_b32 m0, s0
	v_and_b32_e32 v86, 6, v86
	global_load_lds_dwordx4 v[68:69], off
	v_or_b32_e32 v68, s38, v74
	v_ashrrev_i32_e32 v69, 31, v68
	v_lshl_add_u64 v[70:71], s[64:65], 0, v[68:69]
	v_lshlrev_b32_e32 v68, 1, v68
	v_lshlrev_b64 v[70:71], 10, v[70:71]
	v_bitop3_b32 v68, v68, v84, 14 bitop3:0x6c
	v_and_b32_e32 v87, 8, v85
	v_lshl_add_u64 v[70:71], s[82:83], 0, v[70:71]
	v_lshlrev_b32_e32 v68, 4, v68
	v_mov_b32_e32 v69, v3
	v_readlane_b32 s0, v255, 18
	v_lshl_add_u32 v72, v84, 5, 0
	v_bitop3_b32 v84, v86, v84, v87 bitop3:0x36
	v_lshl_add_u64 v[68:69], v[70:71], 0, v[68:69]
	s_mov_b32 m0, s0
	v_lshlrev_b32_e32 v87, 4, v84
	v_lshl_add_u32 v84, v85, 2, 0
	v_lshlrev_b32_e32 v85, 9, v85
	global_load_lds_dwordx4 v[68:69], off
	v_add3_u32 v132, 0, v87, v85
	s_waitcnt vmcnt(0)
	s_waitcnt vmcnt(0) lgkmcnt(0)
	s_barrier
	ds_read_b128 v[76:79], v72 offset:1024
	ds_read_b128 v[68:71], v72 offset:1040
	ds_read_b128 v[80:83], v72 offset:2048
	ds_read_b128 v[72:75], v72 offset:2064
	ds_read_b32 v86, v84
	ds_read_b32 v138, v84 offset:512
	ds_read_b128 v[134:137], v132 offset:4096
	s_movk_i32 s0, 0x60
	s_waitcnt lgkmcnt(4)
	v_mov_b32_e32 v125, v82
	v_mov_b32_e32 v82, v81
	s_waitcnt lgkmcnt(3)
	v_mov_b32_e32 v81, v74
	s_waitcnt lgkmcnt(0)
	v_lshlrev_b32_e32 v123, 16, v135
	v_lshlrev_b32_e32 v122, 16, v134
	v_pk_add_f32 v[122:123], v[122:123], v[86:87] op_sel_hi:[1,0] neg_lo:[0,1] neg_hi:[0,1]
	v_and_b32_e32 v135, 0xffff0000, v135
	v_pk_mul_f32 v[140:141], v[138:139], v[122:123] op_sel_hi:[0,1]
	v_mov_b32_e32 v122, v76
	v_mov_b32_e32 v123, v78
	v_and_b32_e32 v134, 0xffff0000, v134
	v_mov_b32_e32 v78, v77
	v_lshlrev_b32_e32 v77, 16, v137
	v_lshlrev_b32_e32 v76, 16, v136
	v_and_b32_e32 v137, 0xffff0000, v137
	v_and_b32_e32 v136, 0xffff0000, v136
	v_pk_add_f32 v[134:135], v[134:135], v[86:87] op_sel_hi:[1,0] neg_lo:[0,1] neg_hi:[0,1]
	v_pk_add_f32 v[76:77], v[76:77], v[86:87] op_sel_hi:[1,0] neg_lo:[0,1] neg_hi:[0,1]
	v_pk_add_f32 v[86:87], v[136:137], v[86:87] op_sel_hi:[1,0] neg_lo:[0,1] neg_hi:[0,1]
	v_pk_mul_f32 v[142:143], v[138:139], v[76:77] op_sel_hi:[0,1]
	v_mov_b32_e32 v77, v70
	v_pk_mul_f32 v[86:87], v[138:139], v[86:87] op_sel_hi:[0,1]
	v_mov_b32_e32 v70, v69
	v_mov_b32_e32 v74, v73
	v_mov_b32_e32 v124, v80
	v_mov_b32_e32 v76, v68
	v_mov_b32_e32 v80, v72
	v_pk_fma_f32 v[68:69], v[70:71], v[86:87], v[74:75]
	v_pk_fma_f32 v[140:141], v[122:123], v[140:141], v[124:125]
	v_pk_mul_f32 v[134:135], v[138:139], v[134:135] op_sel_hi:[0,1]
	v_pk_fma_f32 v[142:143], v[76:77], v[142:143], v[80:81]
	v_pk_fma_f32 v[134:135], v[78:79], v[134:135], v[82:83]
	v_cvt_pk_bf16_f32 v137, v143, v69
	v_cvt_pk_bf16_f32 v136, v142, v68
	v_cvt_pk_bf16_f32 v135, v141, v135
	v_cvt_pk_bf16_f32 v134, v140, v134
	ds_write_b128 v132, v[134:137] offset:4096
	ds_read_b32 v68, v84 offset:64
	ds_read_b32 v72, v84 offset:576
	ds_read_b128 v[134:137], v132 offset:12288
	s_and_b64 vcc, exec, s[10:11]
	s_waitcnt lgkmcnt(0)
; #define LAS __attribute__((address_space(3)))
; __device__ __forceinline__ unsigned pk2(float lo, float hi) { return f2bf(lo) | (f2bf(hi) << 16); }
; __device__ __forceinline__ void sgu_unit(LAS unsigned char* lds, int unit, const bf16* U, const bf16* VG, const bf16* Wsb, const float* bs, const float* lng, const float* lnb, bf16* YA, const float* stat, int tid_in, int lane_in, int wave, unsigned* probe_words = nullptr) {
;     ...
;         for (int it = 0; it < 8; ++it) { const int jr = it * 16 + rb; const float mu = MU[jr], rs = RS[jr];
;             LAS v4u* cp = (LAS v4u*)(VS + jr * 512 + ((pc ^ sgu_xkey(jr)) * 16));
;             const v4u w = *cp; v4u o;
;             o.x = pk2((__uint_as_float(w.x << 16) - mu) * rs * ga[0] + ba[0], (__uint_as_float(w.x & 0xffff0000u) - mu) * rs * ga[1] + ba[1]);
;             o.y = pk2((__uint_as_float(w.y << 16) - mu) * rs * ga[2] + ba[2], (__uint_as_float(w.y & 0xffff0000u) - mu) * rs * ga[3] + ba[3]);
;             o.z = pk2((__uint_as_float(w.z << 16) - mu) * rs * gb[0] + bb[0], (__uint_as_float(w.z & 0xffff0000u) - mu) * rs * gb[1] + bb[1]);
;             o.w = pk2((__uint_as_float(w.w << 16) - mu) * rs * gb[2] + bb[2], (__uint_as_float(w.w & 0xffff0000u) - mu) * rs * gb[3] + bb[3]);
;             *cp = o; }
	v_lshlrev_b32_e32 v87, 16, v135
	v_lshlrev_b32_e32 v86, 16, v134
	v_and_b32_e32 v135, 0xffff0000, v135
	v_and_b32_e32 v134, 0xffff0000, v134
	v_lshlrev_b32_e32 v139, 16, v137
	v_lshlrev_b32_e32 v138, 16, v136
	v_and_b32_e32 v137, 0xffff0000, v137
	v_and_b32_e32 v136, 0xffff0000, v136
	v_pk_add_f32 v[86:87], v[86:87], v[68:69] op_sel_hi:[1,0] neg_lo:[0,1] neg_hi:[0,1]
	v_pk_add_f32 v[134:135], v[134:135], v[68:69] op_sel_hi:[1,0] neg_lo:[0,1] neg_hi:[0,1]
	v_pk_add_f32 v[138:139], v[138:139], v[68:69] op_sel_hi:[1,0] neg_lo:[0,1] neg_hi:[0,1]
	v_pk_add_f32 v[68:69], v[136:137], v[68:69] op_sel_hi:[1,0] neg_lo:[0,1] neg_hi:[0,1]
	v_pk_mul_f32 v[134:135], v[72:73], v[134:135] op_sel_hi:[0,1]
	v_pk_mul_f32 v[68:69], v[72:73], v[68:69] op_sel_hi:[0,1]
	v_pk_mul_f32 v[86:87], v[72:73], v[86:87] op_sel_hi:[0,1]
	v_pk_fma_f32 v[134:135], v[78:79], v[134:135], v[82:83]
	v_pk_mul_f32 v[138:139], v[72:73], v[138:139] op_sel_hi:[0,1]
	v_pk_fma_f32 v[68:69], v[70:71], v[68:69], v[74:75]
	v_pk_fma_f32 v[86:87], v[122:123], v[86:87], v[124:125]
	v_pk_fma_f32 v[138:139], v[76:77], v[138:139], v[80:81]
	v_cvt_pk_bf16_f32 v137, v139, v69
	v_cvt_pk_bf16_f32 v136, v138, v68
	v_cvt_pk_bf16_f32 v135, v87, v135
	v_cvt_pk_bf16_f32 v134, v86, v134
	ds_write_b128 v132, v[134:137] offset:12288
	ds_read_b32 v68, v84 offset:128
	ds_read_b32 v72, v84 offset:640
	ds_read_b128 v[134:137], v132 offset:20480
	s_waitcnt lgkmcnt(0)
	v_lshlrev_b32_e32 v87, 16, v135
	v_lshlrev_b32_e32 v86, 16, v134
	v_and_b32_e32 v135, 0xffff0000, v135
	v_and_b32_e32 v134, 0xffff0000, v134
	v_lshlrev_b32_e32 v139, 16, v137
	v_lshlrev_b32_e32 v138, 16, v136
	v_and_b32_e32 v137, 0xffff0000, v137
	v_and_b32_e32 v136, 0xffff0000, v136
	v_pk_add_f32 v[86:87], v[86:87], v[68:69] op_sel_hi:[1,0] neg_lo:[0,1] neg_hi:[0,1]
	v_pk_add_f32 v[134:135], v[134:135], v[68:69] op_sel_hi:[1,0] neg_lo:[0,1] neg_hi:[0,1]
	v_pk_add_f32 v[138:139], v[138:139], v[68:69] op_sel_hi:[1,0] neg_lo:[0,1] neg_hi:[0,1]
	v_pk_add_f32 v[68:69], v[136:137], v[68:69] op_sel_hi:[1,0] neg_lo:[0,1] neg_hi:[0,1]
	v_pk_mul_f32 v[134:135], v[72:73], v[134:135] op_sel_hi:[0,1]
	v_pk_mul_f32 v[68:69], v[72:73], v[68:69] op_sel_hi:[0,1]
	v_pk_mul_f32 v[86:87], v[72:73], v[86:87] op_sel_hi:[0,1]
	v_pk_fma_f32 v[134:135], v[78:79], v[134:135], v[82:83]
	v_pk_mul_f32 v[138:139], v[72:73], v[138:139] op_sel_hi:[0,1]
	v_pk_fma_f32 v[68:69], v[70:71], v[68:69], v[74:75]
	v_pk_fma_f32 v[86:87], v[122:123], v[86:87], v[124:125]
	v_pk_fma_f32 v[138:139], v[76:77], v[138:139], v[80:81]
	v_cvt_pk_bf16_f32 v137, v139, v69
	v_cvt_pk_bf16_f32 v136, v138, v68
	v_cvt_pk_bf16_f32 v135, v87, v135
	v_cvt_pk_bf16_f32 v134, v86, v134
	ds_write_b128 v132, v[134:137] offset:20480
	ds_read_b32 v68, v84 offset:192
	ds_read_b32 v72, v84 offset:704
	ds_read_b128 v[134:137], v132 offset:28672
	s_waitcnt lgkmcnt(0)
	v_lshlrev_b32_e32 v87, 16, v135
	v_lshlrev_b32_e32 v86, 16, v134
	v_and_b32_e32 v135, 0xffff0000, v135
	v_and_b32_e32 v134, 0xffff0000, v134
	v_lshlrev_b32_e32 v139, 16, v137
	v_lshlrev_b32_e32 v138, 16, v136
	v_and_b32_e32 v137, 0xffff0000, v137
	v_and_b32_e32 v136, 0xffff0000, v136
	v_pk_add_f32 v[86:87], v[86:87], v[68:69] op_sel_hi:[1,0] neg_lo:[0,1] neg_hi:[0,1]
	v_pk_add_f32 v[134:135], v[134:135], v[68:69] op_sel_hi:[1,0] neg_lo:[0,1] neg_hi:[0,1]
	v_pk_add_f32 v[138:139], v[138:139], v[68:69] op_sel_hi:[1,0] neg_lo:[0,1] neg_hi:[0,1]
	v_pk_add_f32 v[68:69], v[136:137], v[68:69] op_sel_hi:[1,0] neg_lo:[0,1] neg_hi:[0,1]
	v_pk_mul_f32 v[134:135], v[72:73], v[134:135] op_sel_hi:[0,1]
	v_pk_mul_f32 v[68:69], v[72:73], v[68:69] op_sel_hi:[0,1]
	v_pk_mul_f32 v[86:87], v[72:73], v[86:87] op_sel_hi:[0,1]
	v_pk_fma_f32 v[134:135], v[78:79], v[134:135], v[82:83]
	v_pk_mul_f32 v[138:139], v[72:73], v[138:139] op_sel_hi:[0,1]
	v_pk_fma_f32 v[68:69], v[70:71], v[68:69], v[74:75]
	v_pk_fma_f32 v[86:87], v[122:123], v[86:87], v[124:125]
	v_pk_fma_f32 v[138:139], v[76:77], v[138:139], v[80:81]
	v_cvt_pk_bf16_f32 v137, v139, v69
	v_cvt_pk_bf16_f32 v136, v138, v68
	v_cvt_pk_bf16_f32 v135, v87, v135
	v_cvt_pk_bf16_f32 v134, v86, v134
	ds_write_b128 v132, v[134:137] offset:28672
	ds_read_b32 v68, v84 offset:256
	ds_read_b32 v72, v84 offset:768
	ds_read_b128 v[134:137], v132 offset:36864
	s_waitcnt lgkmcnt(0)
	v_lshlrev_b32_e32 v87, 16, v135
	v_lshlrev_b32_e32 v86, 16, v134
	v_and_b32_e32 v135, 0xffff0000, v135
	v_and_b32_e32 v134, 0xffff0000, v134
	v_lshlrev_b32_e32 v139, 16, v137
	v_lshlrev_b32_e32 v138, 16, v136
	v_and_b32_e32 v137, 0xffff0000, v137
	v_and_b32_e32 v136, 0xffff0000, v136
	v_pk_add_f32 v[86:87], v[86:87], v[68:69] op_sel_hi:[1,0] neg_lo:[0,1] neg_hi:[0,1]
	v_pk_add_f32 v[134:135], v[134:135], v[68:69] op_sel_hi:[1,0] neg_lo:[0,1] neg_hi:[0,1]
	v_pk_add_f32 v[138:139], v[138:139], v[68:69] op_sel_hi:[1,0] neg_lo:[0,1] neg_hi:[0,1]
	v_pk_add_f32 v[68:69], v[136:137], v[68:69] op_sel_hi:[1,0] neg_lo:[0,1] neg_hi:[0,1]
	v_pk_mul_f32 v[134:135], v[72:73], v[134:135] op_sel_hi:[0,1]
	v_pk_mul_f32 v[68:69], v[72:73], v[68:69] op_sel_hi:[0,1]
	v_pk_mul_f32 v[86:87], v[72:73], v[86:87] op_sel_hi:[0,1]
	v_pk_fma_f32 v[134:135], v[78:79], v[134:135], v[82:83]
	v_pk_mul_f32 v[138:139], v[72:73], v[138:139] op_sel_hi:[0,1]
	v_pk_fma_f32 v[68:69], v[70:71], v[68:69], v[74:75]
	v_pk_fma_f32 v[86:87], v[122:123], v[86:87], v[124:125]
	v_pk_fma_f32 v[138:139], v[76:77], v[138:139], v[80:81]
	v_cvt_pk_bf16_f32 v137, v139, v69
	v_cvt_pk_bf16_f32 v136, v138, v68
	v_cvt_pk_bf16_f32 v135, v87, v135
	v_cvt_pk_bf16_f32 v134, v86, v134
	ds_write_b128 v132, v[134:137] offset:36864
	ds_read_b32 v68, v84 offset:320
	ds_read_b32 v72, v84 offset:832
	ds_read_b128 v[134:137], v132 offset:45056
	s_waitcnt lgkmcnt(0)
; #define LAS __attribute__((address_space(3)))
; __device__ __forceinline__ unsigned pk2(float lo, float hi) { return f2bf(lo) | (f2bf(hi) << 16); }
; #define SPROBE(k) do { const unsigned long long tn_ = __builtin_amdgcn_s_memrealtime(); if (blockIdx.x == 0 && threadIdx.x == 0) atomicAdd(probe_words + (k), (unsigned)(tn_ - tp0_)); tp0_ = tn_; } while (0)
; #define SPROBE(k) do {} while (0)
; __device__ __forceinline__ void sgu_unit(LAS unsigned char* lds, int unit, const bf16* U, const bf16* VG, const bf16* Wsb, const float* bs, const float* lng, const float* lnb, bf16* YA, const float* stat, int tid_in, int lane_in, int wave, unsigned* probe_words = nullptr) {
;     ...
;         for (int it = 0; it < 8; ++it) { const int jr = it * 16 + rb; const float mu = MU[jr], rs = RS[jr];
;             LAS v4u* cp = (LAS v4u*)(VS + jr * 512 + ((pc ^ sgu_xkey(jr)) * 16));
;             const v4u w = *cp; v4u o;
;             o.x = pk2((__uint_as_float(w.x << 16) - mu) * rs * ga[0] + ba[0], (__uint_as_float(w.x & 0xffff0000u) - mu) * rs * ga[1] + ba[1]);
;             o.y = pk2((__uint_as_float(w.y << 16) - mu) * rs * ga[2] + ba[2], (__uint_as_float(w.y & 0xffff0000u) - mu) * rs * ga[3] + ba[3]);
;             o.z = pk2((__uint_as_float(w.z << 16) - mu) * rs * gb[0] + bb[0], (__uint_as_float(w.z & 0xffff0000u) - mu) * rs * gb[1] + bb[1]);
;             o.w = pk2((__uint_as_float(w.w << 16) - mu) * rs * gb[2] + bb[2], (__uint_as_float(w.w & 0xffff0000u) - mu) * rs * gb[3] + bb[3]);
;             *cp = o; }
;     }
;     __syncthreads();
;     SPROBE(6);
;     {
;         const int tq = (lane & 15) >> 2, tp = lane & 3; const int xkp = sgu_xkey(8 * q4 + tq) ^ (tp >> 1);
;         const LAS unsigned char* tb = VS + (8 * q4 + tq) * 512 + 8 * (tp & 1);
; #pragma unroll
;         for (int gi = 0; gi < 4; ++gi) {
;             const int g = half * 4 + gi;
;             f32x4s acc[4];
; #pragma unroll
;             for (int nn = 0; nn < 4; ++nn) acc[nn] = (f32x4s){0.f, 0.f, 0.f, 0.f};
	v_lshlrev_b32_e32 v87, 16, v135
	v_lshlrev_b32_e32 v86, 16, v134
	v_and_b32_e32 v135, 0xffff0000, v135
	v_and_b32_e32 v134, 0xffff0000, v134
	v_lshlrev_b32_e32 v139, 16, v137
	v_lshlrev_b32_e32 v138, 16, v136
	v_and_b32_e32 v137, 0xffff0000, v137
	v_and_b32_e32 v136, 0xffff0000, v136
	v_pk_add_f32 v[86:87], v[86:87], v[68:69] op_sel_hi:[1,0] neg_lo:[0,1] neg_hi:[0,1]
	v_pk_add_f32 v[134:135], v[134:135], v[68:69] op_sel_hi:[1,0] neg_lo:[0,1] neg_hi:[0,1]
	v_pk_add_f32 v[138:139], v[138:139], v[68:69] op_sel_hi:[1,0] neg_lo:[0,1] neg_hi:[0,1]
	v_pk_add_f32 v[68:69], v[136:137], v[68:69] op_sel_hi:[1,0] neg_lo:[0,1] neg_hi:[0,1]
	v_pk_mul_f32 v[134:135], v[72:73], v[134:135] op_sel_hi:[0,1]
	v_pk_mul_f32 v[68:69], v[72:73], v[68:69] op_sel_hi:[0,1]
	v_pk_mul_f32 v[86:87], v[72:73], v[86:87] op_sel_hi:[0,1]
	v_pk_fma_f32 v[134:135], v[78:79], v[134:135], v[82:83]
	v_pk_mul_f32 v[138:139], v[72:73], v[138:139] op_sel_hi:[0,1]
	v_pk_fma_f32 v[68:69], v[70:71], v[68:69], v[74:75]
	v_pk_fma_f32 v[86:87], v[122:123], v[86:87], v[124:125]
	v_pk_fma_f32 v[138:139], v[76:77], v[138:139], v[80:81]
	v_cvt_pk_bf16_f32 v137, v139, v69
	v_cvt_pk_bf16_f32 v136, v138, v68
	v_cvt_pk_bf16_f32 v135, v87, v135
	v_cvt_pk_bf16_f32 v134, v86, v134
	ds_write_b128 v132, v[134:137] offset:45056
	ds_read_b32 v68, v84 offset:384
	ds_read_b32 v72, v84 offset:896
	ds_read_b128 v[134:137], v132 offset:53248
	s_waitcnt lgkmcnt(0)
	v_lshlrev_b32_e32 v87, 16, v135
	v_lshlrev_b32_e32 v86, 16, v134
	v_and_b32_e32 v135, 0xffff0000, v135
	v_and_b32_e32 v134, 0xffff0000, v134
	v_lshlrev_b32_e32 v139, 16, v137
	v_lshlrev_b32_e32 v138, 16, v136
	v_and_b32_e32 v137, 0xffff0000, v137
	v_and_b32_e32 v136, 0xffff0000, v136
	v_pk_add_f32 v[86:87], v[86:87], v[68:69] op_sel_hi:[1,0] neg_lo:[0,1] neg_hi:[0,1]
	v_pk_add_f32 v[134:135], v[134:135], v[68:69] op_sel_hi:[1,0] neg_lo:[0,1] neg_hi:[0,1]
	v_pk_add_f32 v[138:139], v[138:139], v[68:69] op_sel_hi:[1,0] neg_lo:[0,1] neg_hi:[0,1]
	v_pk_add_f32 v[68:69], v[136:137], v[68:69] op_sel_hi:[1,0] neg_lo:[0,1] neg_hi:[0,1]
	v_pk_mul_f32 v[134:135], v[72:73], v[134:135] op_sel_hi:[0,1]
	v_pk_mul_f32 v[68:69], v[72:73], v[68:69] op_sel_hi:[0,1]
	v_pk_mul_f32 v[86:87], v[72:73], v[86:87] op_sel_hi:[0,1]
	v_pk_fma_f32 v[134:135], v[78:79], v[134:135], v[82:83]
	v_pk_mul_f32 v[138:139], v[72:73], v[138:139] op_sel_hi:[0,1]
	v_pk_fma_f32 v[68:69], v[70:71], v[68:69], v[74:75]
	v_pk_fma_f32 v[86:87], v[122:123], v[86:87], v[124:125]
	v_pk_fma_f32 v[138:139], v[76:77], v[138:139], v[80:81]
	v_cvt_pk_bf16_f32 v137, v139, v69
	v_cvt_pk_bf16_f32 v136, v138, v68
	v_cvt_pk_bf16_f32 v135, v87, v135
	v_cvt_pk_bf16_f32 v134, v86, v134
	ds_write_b128 v132, v[134:137] offset:53248
	ds_read_b32 v68, v84 offset:448
	ds_read_b32 v72, v84 offset:960
	ds_read_b128 v[84:87], v132 offset:61440
	s_waitcnt lgkmcnt(0)
	v_lshlrev_b32_e32 v135, 16, v85
	v_lshlrev_b32_e32 v134, 16, v84
	v_and_b32_e32 v85, 0xffff0000, v85
	v_and_b32_e32 v84, 0xffff0000, v84
	v_pk_add_f32 v[84:85], v[84:85], v[68:69] op_sel_hi:[1,0] neg_lo:[0,1] neg_hi:[0,1]
	v_pk_add_f32 v[134:135], v[134:135], v[68:69] op_sel_hi:[1,0] neg_lo:[0,1] neg_hi:[0,1]
	v_pk_mul_f32 v[84:85], v[72:73], v[84:85] op_sel_hi:[0,1]
	v_pk_fma_f32 v[78:79], v[78:79], v[84:85], v[82:83]
	v_lshlrev_b32_e32 v83, 16, v87
	v_lshlrev_b32_e32 v82, 16, v86
	v_pk_add_f32 v[82:83], v[82:83], v[68:69] op_sel_hi:[1,0] neg_lo:[0,1] neg_hi:[0,1]
	v_pk_mul_f32 v[134:135], v[72:73], v[134:135] op_sel_hi:[0,1]
	v_pk_mul_f32 v[82:83], v[72:73], v[82:83] op_sel_hi:[0,1]
	v_pk_fma_f32 v[76:77], v[76:77], v[82:83], v[80:81]
	v_and_b32_e32 v81, 0xffff0000, v87
	v_and_b32_e32 v80, 0xffff0000, v86
	v_pk_add_f32 v[68:69], v[80:81], v[68:69] op_sel_hi:[1,0] neg_lo:[0,1] neg_hi:[0,1]
	v_pk_fma_f32 v[122:123], v[122:123], v[134:135], v[124:125]
	v_pk_mul_f32 v[68:69], v[72:73], v[68:69] op_sel_hi:[0,1]
	v_pk_fma_f32 v[68:69], v[70:71], v[68:69], v[74:75]
	v_cvt_pk_bf16_f32 v71, v77, v69
	v_cvt_pk_bf16_f32 v70, v76, v68
	v_cvt_pk_bf16_f32 v69, v123, v79
	v_cvt_pk_bf16_f32 v68, v122, v78
	ds_write_b128 v132, v[68:71] offset:61440
	v_lshrrev_b32_e32 v68, 2, v131
	v_or_b32_e32 v69, v2, v68
	v_lshlrev_b32_e32 v68, 1, v68
	v_and_b32_e32 v2, 8, v2
	v_bfe_u32 v70, v130, 1, 1
	v_or3_b32 v2, v2, v68, v70
	v_lshlrev_b32_e32 v68, 9, v69
	v_lshlrev_b32_e32 v69, 3, v130
	v_and_b32_e32 v69, 8, v69
	v_add3_u32 v125, 0, v68, v69
	v_mov_b32_e32 v84, 0
	v_lshlrev_b32_e32 v130, 4, v2
	v_add_u32_e32 v124, v125, v130
	v_xad_u32 v123, v130, 32, v125
	v_xad_u32 v122, v130, 64, v125
	v_xad_u32 v2, v130, s0, v125
	v_mov_b32_e32 v85, 0
	v_mov_b32_e32 v86, 0
	v_mov_b32_e32 v87, 0
	v_mov_b32_e32 v76, 0
	v_mov_b32_e32 v77, v84
	v_mov_b32_e32 v78, v84
	v_mov_b32_e32 v79, v84
	v_mov_b32_e32 v72, v84
	v_mov_b32_e32 v73, v84
	v_mov_b32_e32 v74, v84
	v_mov_b32_e32 v75, v84
	v_mov_b32_e32 v68, v84
	v_mov_b32_e32 v69, v84
	v_mov_b32_e32 v70, v84
	v_mov_b32_e32 v71, v84
	v_mov_b32_e32 v80, v84
	v_mov_b32_e32 v81, v84
	v_mov_b32_e32 v82, v84
	v_mov_b32_e32 v83, v84
	s_waitcnt lgkmcnt(0)
	s_barrier
	s_cbranch_vccz .LBB0_1016
	s_and_b64 vcc, exec, s[8:9]
	s_cbranch_vccz .LBB0_1017

; #define GAS __attribute__((address_space(1)))
; __device__ __forceinline__ unsigned pk2(float lo, float hi) { return f2bf(lo) | (f2bf(hi) << 16); }
; __device__ __forceinline__ void sgu_unit(LAS unsigned char* lds, int unit, const bf16* U, const bf16* VG, const bf16* Wsb, const float* bs, const float* lng, const float* lnb, bf16* YA, const float* stat, int tid_in, int lane_in, int wave, unsigned* probe_words = nullptr) {
;     ...
;             f32x4s acc[4];
; #pragma unroll
;             for (int nn = 0; nn < 4; ++nn) acc[nn] = (f32x4s){0.f, 0.f, 0.f, 0.f};
;     ...
;             for (int nn = 0; nn < 4; ++nn) { const size_t off = (row0 + irow) * GW + g * GMD + 16 * nn + 4 * q4;
;                 const unsigned u0 = (unsigned)uw[gi][nn], u1 = (unsigned)(uw[gi][nn] >> 32);
;                 const float y0 = __uint_as_float(u0 << 16) * (acc[nn][0] + bsv[gi]), y1 = __uint_as_float(u0 & 0xffff0000u) * (acc[nn][1] + bsv[gi]), y2 = __uint_as_float(u1 << 16) * (acc[nn][2] + bsv[gi]), y3 = __uint_as_float(u1 & 0xffff0000u) * (acc[nn][3] + bsv[gi]);
;                 *(GAS unsigned long long*)(YA + off) = (unsigned long long)pk2(y0, y1) | ((unsigned long long)pk2(y2, y3) << 32); }
.LBB0_998:
	v_lshlrev_b32_e32 v52, 16, v120
	v_add_f32_e32 v53, v129, v76
	v_mul_f32_e32 v52, v53, v52
	v_and_b32_e32 v53, 0xffff0000, v120
	v_add_f32_e32 v54, v129, v77
	v_mul_f32_e32 v53, v54, v53
	v_lshlrev_b32_e32 v54, 16, v121
	v_add_f32_e32 v55, v129, v78
	v_mul_f32_e32 v54, v55, v54
	v_and_b32_e32 v55, 0xffff0000, v121
	v_add_f32_e32 v56, v129, v79
	v_mul_f32_e32 v55, v56, v55
	v_cvt_pk_bf16_f32 v52, v52, v53
	v_cvt_pk_bf16_f32 v53, v54, v55
	global_store_dwordx2 v[88:89], v[52:53], off
	v_lshlrev_b32_e32 v52, 16, v118
	v_add_f32_e32 v53, v129, v72
	v_mul_f32_e32 v52, v53, v52
	v_and_b32_e32 v53, 0xffff0000, v118
	v_add_f32_e32 v54, v129, v73
	v_mul_f32_e32 v53, v54, v53
	v_lshlrev_b32_e32 v54, 16, v119
	v_add_f32_e32 v55, v129, v74
	v_mul_f32_e32 v54, v55, v54
	v_and_b32_e32 v55, 0xffff0000, v119
	v_add_f32_e32 v56, v129, v75
	v_mul_f32_e32 v55, v56, v55
	v_cvt_pk_bf16_f32 v52, v52, v53
	v_cvt_pk_bf16_f32 v53, v54, v55
	global_store_dwordx2 v[88:89], v[52:53], off offset:32
	v_lshlrev_b32_e32 v52, 16, v116
	v_add_f32_e32 v53, v129, v68
	v_mul_f32_e32 v52, v53, v52
	v_and_b32_e32 v53, 0xffff0000, v116
	v_add_f32_e32 v54, v129, v69
	v_mul_f32_e32 v53, v54, v53
	v_lshlrev_b32_e32 v54, 16, v117
	v_add_f32_e32 v55, v129, v70
	v_mul_f32_e32 v54, v55, v54
	v_and_b32_e32 v55, 0xffff0000, v117
	v_add_f32_e32 v56, v129, v71
	v_mul_f32_e32 v55, v56, v55
	v_cvt_pk_bf16_f32 v52, v52, v53
	v_cvt_pk_bf16_f32 v53, v54, v55
	global_store_dwordx2 v[88:89], v[52:53], off offset:64
	v_lshlrev_b32_e32 v52, 16, v114
	v_add_f32_e32 v53, v129, v80
	v_mul_f32_e32 v52, v53, v52
	v_and_b32_e32 v53, 0xffff0000, v114
	v_add_f32_e32 v54, v129, v81
	v_mul_f32_e32 v53, v54, v53
	v_lshlrev_b32_e32 v54, 16, v115
	v_add_f32_e32 v55, v129, v82
	v_mul_f32_e32 v54, v55, v54
	v_and_b32_e32 v55, 0xffff0000, v115
	v_add_f32_e32 v56, v129, v83
	v_mul_f32_e32 v55, v56, v55
	v_cvt_pk_bf16_f32 v52, v52, v53
	s_movk_i32 s0, 0x80
	v_xad_u32 v75, v130, s0, v125
	s_movk_i32 s0, 0xa0
	v_xad_u32 v74, v130, s0, v125
	s_movk_i32 s0, 0xc0
	v_cvt_pk_bf16_f32 v53, v54, v55
	v_mov_b32_e32 v68, 0
	v_xad_u32 v73, v130, s0, v125
	s_movk_i32 s0, 0xe0
	global_store_dwordx2 v[88:89], v[52:53], off offset:96
	s_and_b64 vcc, exec, s[10:11]
	v_xad_u32 v72, v130, s0, v125
	v_mov_b32_e32 v69, 0
	v_mov_b32_e32 v70, 0
	v_mov_b32_e32 v71, 0
	v_mov_b32_e32 v60, 0
	v_mov_b32_e32 v61, v68
	v_mov_b32_e32 v62, v68
	v_mov_b32_e32 v63, v68
	v_mov_b32_e32 v56, v68
	v_mov_b32_e32 v57, v68
	v_mov_b32_e32 v58, v68
	v_mov_b32_e32 v59, v68
	v_mov_b32_e32 v52, v68
	v_mov_b32_e32 v53, v68
	v_mov_b32_e32 v54, v68
	v_mov_b32_e32 v55, v68
	v_mov_b32_e32 v64, v68
	v_mov_b32_e32 v65, v68
	v_mov_b32_e32 v66, v68
	v_mov_b32_e32 v67, v68
	s_cbranch_vccz .LBB0_1019
	s_and_b64 vcc, exec, s[8:9]
	s_cbranch_vccz .LBB0_1020

; #define GAS __attribute__((address_space(1)))
; __device__ __forceinline__ unsigned pk2(float lo, float hi) { return f2bf(lo) | (f2bf(hi) << 16); }
; __device__ __forceinline__ void sgu_unit(LAS unsigned char* lds, int unit, const bf16* U, const bf16* VG, const bf16* Wsb, const float* bs, const float* lng, const float* lnb, bf16* YA, const float* stat, int tid_in, int lane_in, int wave, unsigned* probe_words = nullptr) {
;     ...
;             f32x4s acc[4];
; #pragma unroll
;             for (int nn = 0; nn < 4; ++nn) acc[nn] = (f32x4s){0.f, 0.f, 0.f, 0.f};
;     ...
;             for (int nn = 0; nn < 4; ++nn) { const size_t off = (row0 + irow) * GW + g * GMD + 16 * nn + 4 * q4;
;                 const unsigned u0 = (unsigned)uw[gi][nn], u1 = (unsigned)(uw[gi][nn] >> 32);
;                 const float y0 = __uint_as_float(u0 << 16) * (acc[nn][0] + bsv[gi]), y1 = __uint_as_float(u0 & 0xffff0000u) * (acc[nn][1] + bsv[gi]), y2 = __uint_as_float(u1 << 16) * (acc[nn][2] + bsv[gi]), y3 = __uint_as_float(u1 & 0xffff0000u) * (acc[nn][3] + bsv[gi]);
;                 *(GAS unsigned long long*)(YA + off) = (unsigned long long)pk2(y0, y1) | ((unsigned long long)pk2(y2, y3) << 32); }
.LBB0_1003:
	v_lshlrev_b32_e32 v36, 16, v112
	v_add_f32_e32 v37, v128, v60
	v_mul_f32_e32 v36, v37, v36
	v_and_b32_e32 v37, 0xffff0000, v112
	v_add_f32_e32 v38, v128, v61
	v_mul_f32_e32 v37, v38, v37
	v_lshlrev_b32_e32 v38, 16, v113
	v_add_f32_e32 v39, v128, v62
	v_mul_f32_e32 v38, v39, v38
	v_and_b32_e32 v39, 0xffff0000, v113
	v_add_f32_e32 v40, v128, v63
	v_mul_f32_e32 v39, v40, v39
	v_cvt_pk_bf16_f32 v36, v36, v37
	v_cvt_pk_bf16_f32 v37, v38, v39
	global_store_dwordx2 v[88:89], v[36:37], off offset:128
	v_lshlrev_b32_e32 v36, 16, v110
	v_add_f32_e32 v37, v128, v56
	v_mul_f32_e32 v36, v37, v36
	v_and_b32_e32 v37, 0xffff0000, v110
	v_add_f32_e32 v38, v128, v57
	v_mul_f32_e32 v37, v38, v37
	v_lshlrev_b32_e32 v38, 16, v111
	v_add_f32_e32 v39, v128, v58
	v_mul_f32_e32 v38, v39, v38
	v_and_b32_e32 v39, 0xffff0000, v111
	v_add_f32_e32 v40, v128, v59
	v_mul_f32_e32 v39, v40, v39
	v_cvt_pk_bf16_f32 v36, v36, v37
	v_cvt_pk_bf16_f32 v37, v38, v39
	global_store_dwordx2 v[88:89], v[36:37], off offset:160
	v_lshlrev_b32_e32 v36, 16, v108
	v_add_f32_e32 v37, v128, v52
	v_mul_f32_e32 v36, v37, v36
	v_and_b32_e32 v37, 0xffff0000, v108
	v_add_f32_e32 v38, v128, v53
	v_mul_f32_e32 v37, v38, v37
	v_lshlrev_b32_e32 v38, 16, v109
	v_add_f32_e32 v39, v128, v54
	v_mul_f32_e32 v38, v39, v38
	v_and_b32_e32 v39, 0xffff0000, v109
	v_add_f32_e32 v40, v128, v55
	v_mul_f32_e32 v39, v40, v39
	v_cvt_pk_bf16_f32 v36, v36, v37
	v_cvt_pk_bf16_f32 v37, v38, v39
	global_store_dwordx2 v[88:89], v[36:37], off offset:192
	v_lshlrev_b32_e32 v36, 16, v106
	v_add_f32_e32 v37, v128, v64
	v_mul_f32_e32 v36, v37, v36
	v_and_b32_e32 v37, 0xffff0000, v106
	v_add_f32_e32 v38, v128, v65
	v_mul_f32_e32 v37, v38, v37
	v_lshlrev_b32_e32 v38, 16, v107
	v_add_f32_e32 v39, v128, v66
	v_mul_f32_e32 v38, v39, v38
	v_and_b32_e32 v39, 0xffff0000, v107
	v_add_f32_e32 v40, v128, v67
	v_mul_f32_e32 v39, v40, v39
	v_cvt_pk_bf16_f32 v36, v36, v37
	v_cvt_pk_bf16_f32 v37, v38, v39
	v_mov_b32_e32 v52, 0
	global_store_dwordx2 v[88:89], v[36:37], off offset:224
	s_and_b64 vcc, exec, s[10:11]
	v_mov_b32_e32 v53, 0
	v_mov_b32_e32 v54, 0
	v_mov_b32_e32 v55, 0
	v_mov_b32_e32 v44, 0
	v_mov_b32_e32 v45, v52
	v_mov_b32_e32 v46, v52
	v_mov_b32_e32 v47, v52
	v_mov_b32_e32 v40, v52
	v_mov_b32_e32 v41, v52
	v_mov_b32_e32 v42, v52
	v_mov_b32_e32 v43, v52
	v_mov_b32_e32 v36, v52
	v_mov_b32_e32 v37, v52
	v_mov_b32_e32 v38, v52
	v_mov_b32_e32 v39, v52
	v_mov_b32_e32 v48, v52
	v_mov_b32_e32 v49, v52
	v_mov_b32_e32 v50, v52
	v_mov_b32_e32 v51, v52
	s_cbranch_vccz .LBB0_1022
	s_and_b64 vcc, exec, s[8:9]
	s_cbranch_vccz .LBB0_1023

; #define GAS __attribute__((address_space(1)))
; __device__ __forceinline__ unsigned pk2(float lo, float hi) { return f2bf(lo) | (f2bf(hi) << 16); }
; __device__ __forceinline__ void sgu_unit(LAS unsigned char* lds, int unit, const bf16* U, const bf16* VG, const bf16* Wsb, const float* bs, const float* lng, const float* lnb, bf16* YA, const float* stat, int tid_in, int lane_in, int wave, unsigned* probe_words = nullptr) {
;     ...
;             f32x4s acc[4];
; #pragma unroll
;             for (int nn = 0; nn < 4; ++nn) acc[nn] = (f32x4s){0.f, 0.f, 0.f, 0.f};
;     ...
;             for (int nn = 0; nn < 4; ++nn) { const size_t off = (row0 + irow) * GW + g * GMD + 16 * nn + 4 * q4;
;                 const unsigned u0 = (unsigned)uw[gi][nn], u1 = (unsigned)(uw[gi][nn] >> 32);
;                 const float y0 = __uint_as_float(u0 << 16) * (acc[nn][0] + bsv[gi]), y1 = __uint_as_float(u0 & 0xffff0000u) * (acc[nn][1] + bsv[gi]), y2 = __uint_as_float(u1 << 16) * (acc[nn][2] + bsv[gi]), y3 = __uint_as_float(u1 & 0xffff0000u) * (acc[nn][3] + bsv[gi]);
;                 *(GAS unsigned long long*)(YA + off) = (unsigned long long)pk2(y0, y1) | ((unsigned long long)pk2(y2, y3) << 32); }
.LBB0_1008:
	v_lshlrev_b32_e32 v2, 16, v104
	v_add_f32_e32 v20, v127, v44
	v_mul_f32_e32 v2, v20, v2
	v_and_b32_e32 v20, 0xffff0000, v104
	v_add_f32_e32 v21, v127, v45
	v_mul_f32_e32 v20, v21, v20
	v_lshlrev_b32_e32 v21, 16, v105
	v_add_f32_e32 v22, v127, v46
	v_mul_f32_e32 v21, v22, v21
	v_and_b32_e32 v22, 0xffff0000, v105
	v_add_f32_e32 v23, v127, v47
	v_mul_f32_e32 v22, v23, v22
	v_cvt_pk_bf16_f32 v20, v2, v20
	v_cvt_pk_bf16_f32 v21, v21, v22
	global_store_dwordx2 v[88:89], v[20:21], off offset:256
	v_lshlrev_b32_e32 v2, 16, v102
	v_add_f32_e32 v20, v127, v40
	v_mul_f32_e32 v2, v20, v2
	v_and_b32_e32 v20, 0xffff0000, v102
	v_add_f32_e32 v21, v127, v41
	v_mul_f32_e32 v20, v21, v20
	v_lshlrev_b32_e32 v21, 16, v103
	v_add_f32_e32 v22, v127, v42
	v_mul_f32_e32 v21, v22, v21
	v_and_b32_e32 v22, 0xffff0000, v103
	v_add_f32_e32 v23, v127, v43
	v_mul_f32_e32 v22, v23, v22
	v_cvt_pk_bf16_f32 v20, v2, v20
	v_cvt_pk_bf16_f32 v21, v21, v22
	global_store_dwordx2 v[88:89], v[20:21], off offset:288
	v_lshlrev_b32_e32 v2, 16, v100
	v_add_f32_e32 v20, v127, v36
	v_mul_f32_e32 v2, v20, v2
	v_and_b32_e32 v20, 0xffff0000, v100
	v_add_f32_e32 v21, v127, v37
	v_mul_f32_e32 v20, v21, v20
	v_lshlrev_b32_e32 v21, 16, v101
	v_add_f32_e32 v22, v127, v38
	v_mul_f32_e32 v21, v22, v21
	v_and_b32_e32 v22, 0xffff0000, v101
	v_add_f32_e32 v23, v127, v39
	v_mul_f32_e32 v22, v23, v22
	v_cvt_pk_bf16_f32 v20, v2, v20
	v_cvt_pk_bf16_f32 v21, v21, v22
	global_store_dwordx2 v[88:89], v[20:21], off offset:320
	v_lshlrev_b32_e32 v2, 16, v98
	v_add_f32_e32 v20, v127, v48
	v_mul_f32_e32 v2, v20, v2
	v_and_b32_e32 v20, 0xffff0000, v98
	v_add_f32_e32 v21, v127, v49
	v_mul_f32_e32 v20, v21, v20
	v_lshlrev_b32_e32 v21, 16, v99
	v_add_f32_e32 v22, v127, v50
	v_mul_f32_e32 v21, v22, v21
	v_and_b32_e32 v22, 0xffff0000, v99
	v_add_f32_e32 v23, v127, v51
	v_mul_f32_e32 v22, v23, v22
	v_cvt_pk_bf16_f32 v20, v2, v20
	v_cvt_pk_bf16_f32 v21, v21, v22
	v_mov_b32_e32 v36, 0
	global_store_dwordx2 v[88:89], v[20:21], off offset:352
	s_and_b64 vcc, exec, s[10:11]
	v_mov_b32_e32 v37, 0
	v_mov_b32_e32 v38, 0
	v_mov_b32_e32 v39, 0
	v_mov_b32_e32 v28, 0
	v_mov_b32_e32 v29, v36
	v_mov_b32_e32 v30, v36
	v_mov_b32_e32 v31, v36
	v_mov_b32_e32 v24, v36
	v_mov_b32_e32 v25, v36
	v_mov_b32_e32 v26, v36
	v_mov_b32_e32 v27, v36
	v_mov_b32_e32 v20, v36
	v_mov_b32_e32 v21, v36
	v_mov_b32_e32 v22, v36
	v_mov_b32_e32 v23, v36
	v_mov_b32_e32 v32, v36
	v_mov_b32_e32 v33, v36
	v_mov_b32_e32 v34, v36
	v_mov_b32_e32 v35, v36
	s_cbranch_vccz .LBB0_1025
	s_and_b64 vcc, exec, s[8:9]
	s_cbranch_vccz .LBB0_1026

; #define GAS __attribute__((address_space(1)))
; __device__ __forceinline__ unsigned pk2(float lo, float hi) { return f2bf(lo) | (f2bf(hi) << 16); }
; __device__ __forceinline__ void sgu_unit(LAS unsigned char* lds, int unit, const bf16* U, const bf16* VG, const bf16* Wsb, const float* bs, const float* lng, const float* lnb, bf16* YA, const float* stat, int tid_in, int lane_in, int wave, unsigned* probe_words = nullptr) {
;     ...
;             for (int nn = 0; nn < 4; ++nn) { const size_t off = (row0 + irow) * GW + g * GMD + 16 * nn + 4 * q4;
;                 const unsigned u0 = (unsigned)uw[gi][nn], u1 = (unsigned)(uw[gi][nn] >> 32);
;                 const float y0 = __uint_as_float(u0 << 16) * (acc[nn][0] + bsv[gi]), y1 = __uint_as_float(u0 & 0xffff0000u) * (acc[nn][1] + bsv[gi]), y2 = __uint_as_float(u1 << 16) * (acc[nn][2] + bsv[gi]), y3 = __uint_as_float(u1 & 0xffff0000u) * (acc[nn][3] + bsv[gi]);
;                 *(GAS unsigned long long*)(YA + off) = (unsigned long long)pk2(y0, y1) | ((unsigned long long)pk2(y2, y3) << 32); }
;         }
;     }
;     __syncthreads();
.LBB0_1013:
	v_lshlrev_b32_e32 v2, 16, v96
	v_add_f32_e32 v4, v126, v28
	v_mul_f32_e32 v2, v4, v2
	v_and_b32_e32 v4, 0xffff0000, v96
	v_add_f32_e32 v5, v126, v29
	v_mul_f32_e32 v4, v5, v4
	v_lshlrev_b32_e32 v5, 16, v97
	v_add_f32_e32 v6, v126, v30
	v_mul_f32_e32 v5, v6, v5
	v_and_b32_e32 v6, 0xffff0000, v97
	v_add_f32_e32 v7, v126, v31
	v_mul_f32_e32 v6, v7, v6
	v_cvt_pk_bf16_f32 v4, v2, v4
	v_cvt_pk_bf16_f32 v5, v5, v6
	global_store_dwordx2 v[88:89], v[4:5], off offset:384
	v_lshlrev_b32_e32 v2, 16, v94
	v_add_f32_e32 v4, v126, v24
	v_mul_f32_e32 v2, v4, v2
	v_and_b32_e32 v4, 0xffff0000, v94
	v_add_f32_e32 v5, v126, v25
	v_mul_f32_e32 v4, v5, v4
	v_lshlrev_b32_e32 v5, 16, v95
	v_add_f32_e32 v6, v126, v26
	v_mul_f32_e32 v5, v6, v5
	v_and_b32_e32 v6, 0xffff0000, v95
	v_add_f32_e32 v7, v126, v27
	v_mul_f32_e32 v6, v7, v6
	v_cvt_pk_bf16_f32 v4, v2, v4
	v_cvt_pk_bf16_f32 v5, v5, v6
	global_store_dwordx2 v[88:89], v[4:5], off offset:416
	v_lshlrev_b32_e32 v2, 16, v92
	v_add_f32_e32 v4, v126, v20
	v_mul_f32_e32 v2, v4, v2
	v_and_b32_e32 v4, 0xffff0000, v92
	v_add_f32_e32 v5, v126, v21
	v_mul_f32_e32 v4, v5, v4
	v_lshlrev_b32_e32 v5, 16, v93
	v_add_f32_e32 v6, v126, v22
	v_mul_f32_e32 v5, v6, v5
	v_and_b32_e32 v6, 0xffff0000, v93
	v_add_f32_e32 v7, v126, v23
	v_mul_f32_e32 v6, v7, v6
	v_cvt_pk_bf16_f32 v4, v2, v4
	v_cvt_pk_bf16_f32 v5, v5, v6
	global_store_dwordx2 v[88:89], v[4:5], off offset:448
	v_lshlrev_b32_e32 v2, 16, v90
	v_add_f32_e32 v4, v126, v32
	v_mul_f32_e32 v2, v4, v2
	v_and_b32_e32 v4, 0xffff0000, v90
	v_add_f32_e32 v5, v126, v33
	v_mul_f32_e32 v4, v5, v4
	v_lshlrev_b32_e32 v5, 16, v91
	v_add_f32_e32 v6, v126, v34
	v_mul_f32_e32 v5, v6, v5
	v_and_b32_e32 v6, 0xffff0000, v91
	v_add_f32_e32 v7, v126, v35
	v_mul_f32_e32 v6, v7, v6
	v_cvt_pk_bf16_f32 v4, v2, v4
	v_cvt_pk_bf16_f32 v5, v5, v6
	global_store_dwordx2 v[88:89], v[4:5], off offset:480
	s_barrier
